# attention gather blocks rewritten: 12 list reads up front, 32-bit offsets + SGPR base loads (v_lshl_add_u32), two lgkmcnt waits instead of 12; on top of v11
# speedup vs baseline: 1.0224x; 1.0224x over previous
.LBB0_718:
	s_or_b64 exec, exec, s[12:13]
	s_cmp_eq_u32 s18, 2
	s_cselect_b32 s18, 32, 16
	s_lshl_b32 s12, s44, 9
	s_add_i32 s12, s12, 0
	v_lshl_add_u32 v0, v232, 1, s12
	v_lshlrev_b64 v[56:57], 1, v[14:15]
	v_mov_b32_e32 v197, v56
	v_lshl_add_u64 v[2:3], s[42:43], 0, v[56:57]
	v_lshl_add_u32 v70, v233, 1, s12
	ds_read_u16 v14, v0 offset:32768
	ds_read_u16 v22, v0 offset:32800
	ds_read_u16 v30, v0 offset:32832
	s_waitcnt vmcnt(0)
	ds_read_u16 v38, v0 offset:32864
	ds_read_u16 v46, v70 offset:32768
	ds_read_u16 v48, v70 offset:32784
	ds_read_u16 v58, v70 offset:32800
	ds_read_u16 v60, v70 offset:32816
	s_waitcnt lgkmcnt(7)
	v_lshlrev_b32_e32 v0, 9, v14
	v_lshl_add_u64 v[18:19], v[2:3], 0, v[0:1]
	s_waitcnt lgkmcnt(6)
	v_lshlrev_b32_e32 v0, 9, v22
	v_lshl_add_u64 v[26:27], v[2:3], 0, v[0:1]
	s_waitcnt lgkmcnt(5)
	v_lshlrev_b32_e32 v0, 9, v30
	v_lshl_add_u64 v[34:35], v[2:3], 0, v[0:1]
	s_waitcnt lgkmcnt(4)
	v_lshlrev_b32_e32 v0, 9, v38
	v_lshl_add_u64 v[42:43], v[2:3], 0, v[0:1]
	s_waitcnt lgkmcnt(3)
	v_lshlrev_b32_e32 v0, 9, v46
	s_waitcnt lgkmcnt(2)
	v_lshlrev_b32_e32 v48, 9, v48
	v_mov_b32_e32 v49, v1
	v_lshl_add_u64 v[46:47], s[42:43], 0, v[0:1]
	v_and_b32_e32 v0, 0x70, v52
	v_lshl_add_u64 v[48:49], s[42:43], 0, v[48:49]
	v_lshl_add_u64 v[46:47], v[46:47], 0, v[0:1]
	v_lshl_add_u64 v[50:51], v[48:49], 0, v[0:1]
	global_load_dwordx4 v[14:17], v[18:19], off
	s_nop 0
	global_load_dwordx4 v[18:21], v[18:19], off offset:64
	s_nop 0
	global_load_dwordx4 v[22:25], v[26:27], off
	s_nop 0
	global_load_dwordx4 v[26:29], v[26:27], off offset:64
	s_nop 0
	global_load_dwordx4 v[30:33], v[34:35], off
	s_nop 0
	global_load_dwordx4 v[34:37], v[34:35], off offset:64
	s_nop 0
	global_load_dwordx4 v[38:41], v[42:43], off
	s_nop 0
	global_load_dwordx4 v[42:45], v[42:43], off offset:64
	s_nop 0
	global_load_dwordx4 v[46:49], v[46:47], off offset:128
	s_nop 0
	global_load_dwordx4 v[50:53], v[50:51], off offset:128
	s_waitcnt lgkmcnt(1)
	v_lshlrev_b32_e32 v58, 9, v58
	v_mov_b32_e32 v59, v1
	s_waitcnt lgkmcnt(0)
	v_lshlrev_b32_e32 v60, 9, v60
	v_mov_b32_e32 v61, v1
	ds_read_u16 v71, v70 offset:32832
	v_lshl_add_u64 v[58:59], s[42:43], 0, v[58:59]
	v_lshl_add_u64 v[60:61], s[42:43], 0, v[60:61]
	v_lshl_add_u64 v[58:59], v[58:59], 0, v[0:1]
	v_lshl_add_u64 v[60:61], v[60:61], 0, v[0:1]
	global_load_dwordx4 v[62:65], v[58:59], off offset:128
	global_load_dwordx4 v[66:69], v[60:61], off offset:128
	ds_read_u16 v60, v70 offset:32848
	ds_read_u16 v78, v70 offset:32864
	ds_read_u16 v79, v70 offset:32880
	s_waitcnt lgkmcnt(3)
	v_lshlrev_b32_e32 v58, 9, v71
	v_mov_b32_e32 v59, v1
	v_lshl_add_u64 v[58:59], s[42:43], 0, v[58:59]
	s_waitcnt lgkmcnt(2)
	v_lshlrev_b32_e32 v60, 9, v60
	v_mov_b32_e32 v61, v1
	v_lshl_add_u64 v[58:59], v[58:59], 0, v[0:1]
	v_lshl_add_u64 v[60:61], s[42:43], 0, v[60:61]
	v_lshl_add_u64 v[60:61], v[60:61], 0, v[0:1]
	global_load_dwordx4 v[70:73], v[58:59], off offset:128
	global_load_dwordx4 v[74:77], v[60:61], off offset:128
	s_waitcnt lgkmcnt(1)
	v_lshlrev_b32_e32 v58, 9, v78
	v_mov_b32_e32 v59, v1
	v_lshl_add_u64 v[58:59], s[42:43], 0, v[58:59]
	s_waitcnt lgkmcnt(0)
	v_lshlrev_b32_e32 v60, 9, v79
	v_mov_b32_e32 v61, v1
	v_lshl_add_u64 v[58:59], v[58:59], 0, v[0:1]
	v_lshl_add_u64 v[60:61], s[42:43], 0, v[60:61]
	v_lshl_add_u64 v[60:61], v[60:61], 0, v[0:1]
	global_load_dwordx4 v[78:81], v[58:59], off offset:128
	global_load_dwordx4 v[82:85], v[60:61], off offset:128
	v_lshlrev_b32_e32 v5, 6, v5
	s_mov_b32 s47, 2
	v_lshlrev_b32_e32 v210, 2, v54
	v_lshlrev_b32_e32 v54, 4, v233
	v_and_b32_e32 v54, 0x60, v54
	v_xad_u32 v61, v54, v0, s82
	v_lshrrev_b32_e32 v54, 2, v232
	v_or_b32_e32 v54, v210, v54
	v_and_b32_e32 v55, 24, v55
	v_lshlrev_b32_e32 v58, 4, v54
	v_lshl_add_u32 v87, v54, 7, s82
	v_add_u32_e32 v54, 16, v54
	v_lshlrev_b32_e32 v59, 4, v54
	v_lshl_add_u32 v89, v54, 7, s82
	v_or_b32_e32 v92, 32, v55
	s_movk_i32 s12, 0x60
	v_or_b32_e32 v94, 64, v55
	v_mov_b32_e32 v196, v0
	s_mov_b64 s[100:101], s[42:43]
	v_lshl_add_u64 v[212:213], s[42:43], 0, v[0:1]
	v_lshlrev_b32_e32 v0, 1, v5
	v_lshlrev_b32_e32 v60, 7, v233
	v_and_b32_e32 v86, 0x60, v58
	v_and_b32_e32 v88, 0x60, v59
	v_lshlrev_b32_e32 v54, 6, v232
	v_add_u32_e32 v90, v87, v55
	v_add_u32_e32 v91, v89, v55
	v_bitop3_b32 v93, v58, v92, s12 bitop3:0x6c
	v_bitop3_b32 v92, v59, v92, s12 bitop3:0x6c
	v_bitop3_b32 v95, v58, v94, s12 bitop3:0x6c
	v_bitop3_b32 v94, v59, v94, s12 bitop3:0x6c
	v_bitop3_b32 v96, v58, v55, s12 bitop3:0x4e
	v_bitop3_b32 v55, v59, v55, s12 bitop3:0x4e
	v_lshl_add_u64 v[58:59], s[74:75], 0, v[0:1]
	v_mov_b32_e32 v244, 0
	v_ashrrev_i32_e32 v211, 31, v210
	v_lshl_add_u64 v[214:215], v[58:59], 0, v[56:57]
	v_mov_b32_e32 v202, 0xf149f2ca
	v_lshlrev_b32_e32 v216, 1, v54
	v_mov_b32_e32 v5, v4
	v_add_u32_e32 v235, v61, v60
	v_add_u32_e32 v236, v90, v86
	v_add_u32_e32 v237, v91, v88
	v_add_u32_e32 v238, v87, v93
	v_add_u32_e32 v239, v89, v92
	v_add_u32_e32 v240, v87, v95
	v_add_u32_e32 v241, v89, v94
	v_add_u32_e32 v242, v87, v96
	v_add_u32_e32 v243, v89, v55
	v_mov_b32_e32 v154, 0
	v_mov_b32_e32 v155, v244
	v_mov_b32_e32 v156, v244
	v_mov_b32_e32 v157, v244
	v_mov_b32_e32 v158, 0
	v_mov_b32_e32 v159, v244
	v_mov_b32_e32 v160, v244
	v_mov_b32_e32 v161, v244
	v_mov_b32_e32 v162, 0
	v_mov_b32_e32 v163, v244
	v_mov_b32_e32 v164, v244
	v_mov_b32_e32 v165, v244
	v_mov_b32_e32 v166, 0
	v_mov_b32_e32 v167, v244
	v_mov_b32_e32 v168, v244
	v_mov_b32_e32 v169, v244
	s_branch .LBB0_720

.LBB0_720:
	s_add_i32 s12, s47, -2
	s_lshr_b32 s42, s12, 2
	s_add_i32 s42, s42, s44
	s_and_b32 s34, s12, 2
	s_lshl_b32 s12, s42, 9
	s_add_i32 s43, s12, 0
	s_lshl_b32 s12, s34, 7
	s_add_i32 s43, s43, s12
	v_lshl_add_u32 v0, v232, 1, s43
	v_lshl_add_u32 v90, v233, 1, s43
	ds_read_u16 v138, v0 offset:32896
	ds_read_u16 v146, v0 offset:32928
	ds_read_u16 v130, v0 offset:32960
	ds_read_u16 v122, v0 offset:32992
	ds_read_u16 v102, v90 offset:32896
	ds_read_u16 v106, v90 offset:32912
	ds_read_u16 v110, v90 offset:32928
	ds_read_u16 v114, v90 offset:32944
	ds_read_u16 v86, v90 offset:32960
	ds_read_u16 v91, v90 offset:32976
	ds_read_u16 v94, v90 offset:32992
	ds_read_u16 v98, v90 offset:33008
	s_waitcnt lgkmcnt(8)
	v_lshl_add_u32 v142, v138, 9, v197
	v_lshl_add_u32 v134, v146, 9, v197
	v_lshl_add_u32 v126, v130, 9, v197
	v_lshl_add_u32 v118, v122, 9, v197
	global_load_dwordx4 v[138:141], v142, s[100:101]
	global_load_dwordx4 v[142:145], v142, s[100:101] offset:64
	global_load_dwordx4 v[146:149], v134, s[100:101]
	global_load_dwordx4 v[134:137], v134, s[100:101] offset:64
	global_load_dwordx4 v[130:133], v126, s[100:101]
	global_load_dwordx4 v[126:129], v126, s[100:101] offset:64
	global_load_dwordx4 v[122:125], v118, s[100:101]
	global_load_dwordx4 v[118:121], v118, s[100:101] offset:64
	s_waitcnt lgkmcnt(0)
	v_lshl_add_u32 v102, v102, 9, v196
	v_lshl_add_u32 v106, v106, 9, v196
	v_lshl_add_u32 v110, v110, 9, v196
	v_lshl_add_u32 v114, v114, 9, v196
	v_lshl_add_u32 v86, v86, 9, v196
	v_lshl_add_u32 v90, v91, 9, v196
	v_lshl_add_u32 v94, v94, 9, v196
	v_lshl_add_u32 v98, v98, 9, v196
	global_load_dwordx4 v[102:105], v102, s[100:101] offset:128
	global_load_dwordx4 v[106:109], v106, s[100:101] offset:128
	global_load_dwordx4 v[110:113], v110, s[100:101] offset:128
	global_load_dwordx4 v[114:117], v114, s[100:101] offset:128
	global_load_dwordx4 v[86:89], v86, s[100:101] offset:128
	global_load_dwordx4 v[90:93], v90, s[100:101] offset:128
	global_load_dwordx4 v[94:97], v94, s[100:101] offset:128
	global_load_dwordx4 v[98:101], v98, s[100:101] offset:128
	s_cmp_eq_u32 s34, 0
	s_cselect_b64 s[30:31], -1, 0
	s_cmp_lg_u32 s34, 0
	s_cbranch_scc1 .LBB0_722
	v_mov_b32_e32 v244, 0
	v_mov_b32_e32 v202, 0xf149f2ca
	v_mov_b32_e32 v154, 0
	v_mov_b32_e32 v155, v244
	v_mov_b32_e32 v156, v244
	v_mov_b32_e32 v157, v244
	v_mov_b32_e32 v158, 0
	v_mov_b32_e32 v159, v244
	v_mov_b32_e32 v160, v244
	v_mov_b32_e32 v161, v244
	v_mov_b32_e32 v162, 0
	v_mov_b32_e32 v163, v244
	v_mov_b32_e32 v164, v244
	v_mov_b32_e32 v165, v244
	v_mov_b32_e32 v166, 0
	v_mov_b32_e32 v167, v244
	v_mov_b32_e32 v168, v244
	v_mov_b32_e32 v169, v244

.LBB0_745:
	s_lshl_b32 s12, s35, 9
	s_add_i32 s12, s12, 0
	s_lshl_b32 s13, s34, 7
	s_add_i32 s12, s12, s13
	v_lshl_add_u32 v0, v232, 1, s12
	v_lshl_add_u32 v70, v233, 1, s12
	ds_read_u16 v14, v0 offset:32768
	ds_read_u16 v22, v0 offset:32800
	ds_read_u16 v30, v0 offset:32832
	ds_read_u16 v38, v0 offset:32864
	ds_read_u16 v46, v70 offset:32768
	ds_read_u16 v50, v70 offset:32784
	ds_read_u16 v62, v70 offset:32800
	ds_read_u16 v66, v70 offset:32816
	ds_read_u16 v71, v70 offset:32832
	ds_read_u16 v74, v70 offset:32848
	ds_read_u16 v78, v70 offset:32864
	ds_read_u16 v82, v70 offset:32880
	s_waitcnt lgkmcnt(8)
	v_lshl_add_u32 v18, v14, 9, v197
	v_lshl_add_u32 v26, v22, 9, v197
	v_lshl_add_u32 v34, v30, 9, v197
	v_lshl_add_u32 v42, v38, 9, v197
	global_load_dwordx4 v[14:17], v18, s[100:101]
	global_load_dwordx4 v[18:21], v18, s[100:101] offset:64
	global_load_dwordx4 v[22:25], v26, s[100:101]
	global_load_dwordx4 v[26:29], v26, s[100:101] offset:64
	global_load_dwordx4 v[30:33], v34, s[100:101]
	global_load_dwordx4 v[34:37], v34, s[100:101] offset:64
	global_load_dwordx4 v[38:41], v42, s[100:101]
	global_load_dwordx4 v[42:45], v42, s[100:101] offset:64
	s_waitcnt lgkmcnt(0)
	v_lshl_add_u32 v46, v46, 9, v196
	v_lshl_add_u32 v50, v50, 9, v196
	v_lshl_add_u32 v62, v62, 9, v196
	v_lshl_add_u32 v66, v66, 9, v196
	v_lshl_add_u32 v70, v71, 9, v196
	v_lshl_add_u32 v74, v74, 9, v196
	v_lshl_add_u32 v78, v78, 9, v196
	v_lshl_add_u32 v82, v82, 9, v196
	global_load_dwordx4 v[46:49], v46, s[100:101] offset:128
	global_load_dwordx4 v[50:53], v50, s[100:101] offset:128
	global_load_dwordx4 v[62:65], v62, s[100:101] offset:128
	global_load_dwordx4 v[66:69], v66, s[100:101] offset:128
	global_load_dwordx4 v[70:73], v70, s[100:101] offset:128
	global_load_dwordx4 v[74:77], v74, s[100:101] offset:128
	global_load_dwordx4 v[78:81], v78, s[100:101] offset:128
	global_load_dwordx4 v[82:85], v82, s[100:101] offset:128
